# wt4 + attention: next-tile K/V ds_writes spread through the output-scaling section instead of a burst before the barrier
# speedup vs baseline: 1.0162x; 1.0090x over previous
.LBB0_412:
	s_mul_hi_i32 s23, s39, 0x2aaaaaab
	s_lshr_b32 s24, s23, 31
	s_ashr_i32 s23, s23, 5
	s_add_i32 s34, s23, s24
	s_mul_i32 s23, s34, 0xffffff40
	s_add_i32 s23, s39, s23
	s_mov_b32 s31, s25
	s_and_b32 s49, s38, 1
	s_xor_b32 s100, s49, 1
	s_mul_i32 s100, s100, 0x12000
	s_ashr_i32 s24, s23, 6
	s_and_b32 s25, s39, 63
	s_ashr_i32 s36, s34, 4
	s_cmp_eq_u32 s24, 1
	s_cselect_b64 s[26:27], -1, 0
	s_and_b64 s[28:29], s[26:27], exec
	s_cselect_b32 s35, 3, 15
	s_cselect_b32 s37, 2, 4
	s_cmp_lt_u32 s23, 64
	s_cselect_b64 s[28:29], -1, 0
	s_and_b64 s[56:57], s[28:29], exec
	s_cselect_b32 s62, 0, s37
	s_waitcnt vmcnt(2)
	v_mov_b64_e32 v[88:89], v[10:11]
	s_cselect_b32 s23, 0, s35
	s_lshr_b32 s25, s25, s62
	s_waitcnt vmcnt(1)
	v_mov_b64_e32 v[50:51], v[14:15]
	v_mov_b64_e32 v[86:87], v[8:9]
	v_sub_u32_e64 v8, s25, 1 clamp
	v_mov_b64_e32 v[48:49], v[12:13]
	s_ashr_i32 s35, s34, 31
	v_lshlrev_b32_e32 v12, 7, v8
	s_and_b32 s23, s23, s70
	s_lshl_b64 s[56:57], s[34:35], 13
	v_or_b32_e32 v8, v12, v172
	s_or_b32 s56, s56, s23
	v_lshlrev_b32_e32 v64, s62, v8
	v_lshl_add_u64 v[8:9], s[56:57], 0, v[64:65]
	v_lshlrev_b64 v[8:9], 7, v[8:9]
	v_or_b32_e32 v8, v8, v191
	v_lshl_add_u64 v[10:11], s[76:77], 0, v[8:9]
	v_lshl_add_u64 v[8:9], s[78:79], 0, v[8:9]
	global_load_dwordx4 v[16:19], v[10:11], off
	global_load_dwordx4 v[20:23], v[8:9], off
	v_or_b32_e32 v8, v12, v174
	v_lshlrev_b32_e32 v64, s62, v8
	v_lshl_add_u64 v[8:9], s[56:57], 0, v[64:65]
	v_lshlrev_b64 v[8:9], 7, v[8:9]
	v_or_b32_e32 v8, v8, v191
	v_lshl_add_u64 v[10:11], s[76:77], 0, v[8:9]
	v_lshl_add_u64 v[8:9], s[78:79], 0, v[8:9]
	s_lshl_b32 s63, s25, 7
	global_load_dwordx4 v[24:27], v[10:11], off
	global_load_dwordx4 v[28:31], v[8:9], off
	v_or_b32_e32 v8, s63, v172
	v_lshlrev_b32_e32 v64, s62, v8
	v_lshl_add_u64 v[8:9], s[56:57], 0, v[64:65]
	v_lshlrev_b64 v[8:9], 7, v[8:9]
	v_or_b32_e32 v8, v8, v191
	v_lshl_add_u64 v[10:11], s[76:77], 0, v[8:9]
	v_lshl_add_u64 v[8:9], s[78:79], 0, v[8:9]
	global_load_dwordx4 v[32:35], v[10:11], off
	global_load_dwordx4 v[36:39], v[8:9], off
	v_or_b32_e32 v8, s63, v175
	v_lshlrev_b32_e32 v64, s62, v8
	v_lshl_add_u64 v[8:9], s[56:57], 0, v[64:65]
	v_lshlrev_b64 v[8:9], 7, v[8:9]
	v_or_b32_e32 v8, v8, v191
	v_lshl_add_u64 v[10:11], s[76:77], 0, v[8:9]
	v_lshl_add_u64 v[8:9], s[78:79], 0, v[8:9]
	global_load_dwordx4 v[40:43], v[10:11], off
	global_load_dwordx4 v[44:47], v[8:9], off
	s_ashr_i32 s37, s36, 31
	v_add_u32_e32 v8, s63, v181
	s_lshl_b64 s[36:37], s[36:37], 13
	v_ashrrev_i32_e32 v9, 31, v8
	s_or_b32 s36, s36, s23
	v_lshlrev_b64 v[8:9], s62, v[8:9]
	v_lshl_add_u64 v[164:165], s[36:37], 0, v[8:9]
	v_lshlrev_b64 v[162:163], 6, v[164:165]
	s_lshl_b64 s[36:37], s[34:35], 20
	s_add_u32 s36, s64, s36
	v_lshlrev_b32_e32 v8, 1, v162
	s_addc_u32 s37, s65, s37
	v_and_b32_e32 v64, 0xfff80, v8
	v_lshl_add_u64 v[8:9], s[36:37], 0, v[64:65]
	v_mov_b32_e32 v169, v65
	v_lshl_add_u64 v[12:13], v[8:9], 0, v[168:169]
	global_load_dwordx4 v[8:11], v[12:13], off
	s_nop 0
	global_load_dwordx4 v[12:15], v[12:13], off offset:64
	s_mul_i32 s23, s49, 0x12000
	s_add_i32 s23, s23, 0
	v_add3_u32 v56, s23, v182, v215
	v_add3_u32 v64, s23, v183, v215
	ds_read_b128 v[52:55], v56
	ds_read_b128 v[56:59], v56 offset:64
	ds_read_b128 v[60:63], v64
	ds_read_b128 v[66:69], v64 offset:64
	v_add3_u32 v64, s23, v184, v215
	ds_read_b128 v[70:73], v64
	ds_read_b128 v[74:77], v64 offset:64
	v_add3_u32 v64, s23, v185, v215
	ds_read_b128 v[90:93], v64
	ds_read_b128 v[94:97], v64 offset:64
	v_add3_u32 v64, s23, v186, v215
	ds_read_b128 v[98:101], v64
	ds_read_b128 v[102:105], v64 offset:64
	v_add3_u32 v64, s23, v187, v215
	ds_read_b128 v[106:109], v64
	ds_read_b128 v[110:113], v64 offset:64
	v_add3_u32 v64, s23, v188, v215
	ds_read_b128 v[114:117], v64
	ds_read_b128 v[118:121], v64 offset:64
	v_add3_u32 v64, s23, v189, v215
	ds_read_b128 v[122:125], v64
	ds_read_b128 v[126:129], v64 offset:64
	v_add3_u32 v64, s23, v190, v215
	ds_read_b128 v[130:133], v64
	ds_read_b128 v[134:137], v64 offset:64
	s_waitcnt lgkmcnt(14)
	v_mfma_f32_16x16x32_bf16 v[52:55], v[52:55], v[86:89], v[4:7]
	s_cmp_lg_u32 s31, 0
	v_mfma_f32_16x16x32_bf16 v[82:85], v[56:59], v[48:51], v[52:55]
	v_mfma_f32_16x16x32_bf16 v[52:55], v[60:63], v[86:89], 0
	v_mfma_f32_16x16x32_bf16 v[78:81], v[66:69], v[48:51], v[52:55]
	s_waitcnt lgkmcnt(13)
	v_mfma_f32_16x16x32_bf16 v[52:55], v[70:73], v[86:89], 0
	s_waitcnt lgkmcnt(12)
	v_mfma_f32_16x16x32_bf16 v[74:77], v[74:77], v[48:51], v[52:55]
	s_waitcnt lgkmcnt(11)
	v_mfma_f32_16x16x32_bf16 v[52:55], v[90:93], v[86:89], 0
	s_waitcnt lgkmcnt(10)
	v_mfma_f32_16x16x32_bf16 v[70:73], v[94:97], v[48:51], v[52:55]
	s_waitcnt lgkmcnt(9)
	v_mfma_f32_16x16x32_bf16 v[52:55], v[98:101], v[86:89], 0
	s_waitcnt lgkmcnt(8)
	v_mfma_f32_16x16x32_bf16 v[66:69], v[102:105], v[48:51], v[52:55]
	s_waitcnt lgkmcnt(7)
	v_mfma_f32_16x16x32_bf16 v[52:55], v[106:109], v[86:89], 0
	s_waitcnt lgkmcnt(6)
	v_mfma_f32_16x16x32_bf16 v[60:63], v[110:113], v[48:51], v[52:55]
	s_waitcnt lgkmcnt(5)
	v_mfma_f32_16x16x32_bf16 v[52:55], v[114:117], v[86:89], 0
	s_waitcnt lgkmcnt(4)
	v_mfma_f32_16x16x32_bf16 v[56:59], v[118:121], v[48:51], v[52:55]
	s_waitcnt lgkmcnt(3)
	v_mfma_f32_16x16x32_bf16 v[52:55], v[122:125], v[86:89], 0
	s_waitcnt lgkmcnt(1)
	v_mfma_f32_16x16x32_bf16 v[86:89], v[130:133], v[86:89], v[0:3]
	v_mfma_f32_16x16x32_bf16 v[52:55], v[126:129], v[48:51], v[52:55]
	s_waitcnt lgkmcnt(0)
	v_mfma_f32_16x16x32_bf16 v[48:51], v[134:137], v[48:51], v[86:89]
	s_cbranch_scc1 .LBB0_414
	s_nop 3
	v_pk_add_f32 v[86:87], v[84:85], s[84:85] op_sel_hi:[1,0]
	v_pk_add_f32 v[88:89], v[82:83], s[84:85] op_sel_hi:[1,0]
	v_cndmask_b32_e64 v85, v85, v87, s[20:21]
	v_cndmask_b32_e64 v84, v84, v86, s[20:21]
	v_cndmask_b32_e64 v83, v83, v89, s[20:21]
	v_cndmask_b32_e64 v82, v82, v88, s[20:21]
	v_pk_add_f32 v[86:87], v[80:81], s[84:85] op_sel_hi:[1,0]
	v_pk_add_f32 v[88:89], v[78:79], s[84:85] op_sel_hi:[1,0]
	v_cndmask_b32_e64 v81, v81, v87, s[18:19]
	v_cndmask_b32_e64 v80, v80, v86, s[18:19]
	v_cndmask_b32_e64 v79, v79, v89, s[18:19]
	v_cndmask_b32_e64 v78, v78, v88, s[18:19]
	v_pk_add_f32 v[86:87], v[76:77], s[84:85] op_sel_hi:[1,0]
	v_pk_add_f32 v[88:89], v[74:75], s[84:85] op_sel_hi:[1,0]
	v_cndmask_b32_e64 v77, v77, v87, s[16:17]
	v_cndmask_b32_e64 v76, v76, v86, s[16:17]
	v_cndmask_b32_e64 v75, v75, v89, s[16:17]
	v_cndmask_b32_e64 v74, v74, v88, s[16:17]
	v_pk_add_f32 v[86:87], v[72:73], s[84:85] op_sel_hi:[1,0]
	v_pk_add_f32 v[88:89], v[70:71], s[84:85] op_sel_hi:[1,0]
	v_cndmask_b32_e64 v73, v73, v87, s[14:15]
	v_cndmask_b32_e64 v72, v72, v86, s[14:15]
	v_cndmask_b32_e64 v71, v71, v89, s[14:15]
	v_cndmask_b32_e64 v70, v70, v88, s[14:15]
	v_pk_add_f32 v[86:87], v[68:69], s[84:85] op_sel_hi:[1,0]
	v_pk_add_f32 v[88:89], v[66:67], s[84:85] op_sel_hi:[1,0]
	v_cndmask_b32_e64 v69, v69, v87, s[12:13]
	v_cndmask_b32_e64 v68, v68, v86, s[12:13]
	v_cndmask_b32_e64 v67, v67, v89, s[12:13]
	v_cndmask_b32_e64 v66, v66, v88, s[12:13]
	v_pk_add_f32 v[86:87], v[62:63], s[84:85] op_sel_hi:[1,0]
	v_pk_add_f32 v[88:89], v[60:61], s[84:85] op_sel_hi:[1,0]
	v_cndmask_b32_e64 v63, v63, v87, s[10:11]
	v_cndmask_b32_e64 v62, v62, v86, s[10:11]
	v_cndmask_b32_e64 v61, v61, v89, s[10:11]
	v_cndmask_b32_e64 v60, v60, v88, s[10:11]
	v_pk_add_f32 v[86:87], v[58:59], s[84:85] op_sel_hi:[1,0]
	v_pk_add_f32 v[88:89], v[56:57], s[84:85] op_sel_hi:[1,0]
	v_cndmask_b32_e64 v59, v59, v87, s[8:9]
	v_cndmask_b32_e64 v58, v58, v86, s[8:9]
	v_cndmask_b32_e64 v57, v57, v89, s[8:9]
	v_cndmask_b32_e64 v56, v56, v88, s[8:9]
	v_pk_add_f32 v[86:87], v[54:55], s[84:85] op_sel_hi:[1,0]
	v_pk_add_f32 v[88:89], v[52:53], s[84:85] op_sel_hi:[1,0]
	v_cndmask_b32_e64 v55, v55, v87, s[6:7]
	v_cndmask_b32_e64 v54, v54, v86, s[6:7]
	v_cndmask_b32_e64 v53, v53, v89, s[6:7]
	v_cndmask_b32_e64 v52, v52, v88, s[6:7]
.LBB0_414:
	v_add3_u32 v64, s23, v173, v171
	ds_read_b64_tr_b16 v[90:91], v64 offset:36864
	s_nop 1
	ds_read_b64_tr_b16 v[86:87], v64 offset:36896
	ds_read_b64_tr_b16 v[100:101], v64 offset:36928
	ds_read_b64_tr_b16 v[108:109], v64 offset:36960
	ds_read_b64_tr_b16 v[92:93], v64 offset:39168
	ds_read_b64_tr_b16 v[88:89], v64 offset:39200
	ds_read_b64_tr_b16 v[102:103], v64 offset:39232
	ds_read_b64_tr_b16 v[110:111], v64 offset:39264
	ds_read_b64_tr_b16 v[104:105], v64 offset:41472
	ds_read_b64_tr_b16 v[112:113], v64 offset:41504
	ds_read_b64_tr_b16 v[118:119], v64 offset:41536
	ds_read_b64_tr_b16 v[126:127], v64 offset:41568
	ds_read_b64_tr_b16 v[106:107], v64 offset:43776
	ds_read_b64_tr_b16 v[114:115], v64 offset:43808
	ds_read_b64_tr_b16 v[120:121], v64 offset:43840
	ds_read_b64_tr_b16 v[128:129], v64 offset:43872
	ds_read_b64_tr_b16 v[122:123], v64 offset:46080
	ds_read_b64_tr_b16 v[130:131], v64 offset:46112
	ds_read_b64_tr_b16 v[138:139], v64 offset:46144
	ds_read_b64_tr_b16 v[146:147], v64 offset:46176
	ds_read_b64_tr_b16 v[124:125], v64 offset:48384
	ds_read_b64_tr_b16 v[132:133], v64 offset:48416
	ds_read_b64_tr_b16 v[140:141], v64 offset:48448
	ds_read_b64_tr_b16 v[148:149], v64 offset:48480
	ds_read_b64_tr_b16 v[142:143], v64 offset:50688
	ds_read_b64_tr_b16 v[152:153], v64 offset:50720
	ds_read_b64_tr_b16 v[156:157], v64 offset:50752
	ds_read_b64_tr_b16 v[134:135], v64 offset:50784
	ds_read_b64_tr_b16 v[144:145], v64 offset:52992
	ds_read_b64_tr_b16 v[154:155], v64 offset:53024
	ds_read_b64_tr_b16 v[158:159], v64 offset:53056
	ds_read_b64_tr_b16 v[136:137], v64 offset:53088
	ds_read_b64_tr_b16 v[150:151], v64 offset:55296
	ds_read_b64_tr_b16 v[116:117], v64 offset:55328
	ds_read_b64_tr_b16 v[98:99], v64 offset:55360
	ds_read_b64_tr_b16 v[94:95], v64 offset:55392
	v_max3_f32 v64, v82, s84, v83
	v_max3_f32 v64, v64, v84, v85
	v_max3_f32 v64, v64, v78, v79
	v_max3_f32 v64, v64, v80, v81
	v_max3_f32 v64, v64, v74, v75
	v_max3_f32 v64, v64, v76, v77
	v_max3_f32 v64, v64, v70, v71
	v_max3_f32 v64, v64, v72, v73
	v_max3_f32 v64, v64, v66, v67
	v_max3_f32 v64, v64, v68, v69
	v_max3_f32 v64, v64, v60, v61
	v_max3_f32 v64, v64, v62, v63
	v_max3_f32 v64, v64, v56, v57
	v_max3_f32 v64, v64, v58, v59
	v_max3_f32 v64, v64, v52, v53
	v_max3_f32 v64, v64, v54, v55
	v_max3_f32 v64, v64, v48, v49
	v_max3_f32 v64, v64, v50, v51
	v_mov_b32_e32 v96, v64
	s_nop 1
	v_permlane16_swap_b32_e32 v64, v96
	v_max_f32_e32 v96, v96, v96
	v_max_f32_e32 v64, v64, v64
	v_max_f32_e32 v64, v64, v96
	v_mov_b32_e32 v96, v64
	s_nop 1
	v_permlane32_swap_b32_e32 v64, v96
	v_max_f32_e32 v96, v96, v96
	v_max_f32_e32 v64, v64, v64
	v_max_f32_e32 v170, v64, v96
	v_pk_add_f32 v[82:83], v[82:83], v[170:171] op_sel_hi:[1,0] neg_lo:[0,1] neg_hi:[0,1]
	v_pk_add_f32 v[84:85], v[84:85], v[170:171] op_sel_hi:[1,0] neg_lo:[0,1] neg_hi:[0,1]
	v_exp_f32_e32 v82, v82
	v_exp_f32_e32 v83, v83
	v_exp_f32_e32 v84, v84
	v_exp_f32_e32 v85, v85
	v_pk_add_f32 v[78:79], v[78:79], v[170:171] op_sel_hi:[1,0] neg_lo:[0,1] neg_hi:[0,1]
	v_pk_add_f32 v[80:81], v[80:81], v[170:171] op_sel_hi:[1,0] neg_lo:[0,1] neg_hi:[0,1]
	v_exp_f32_e32 v78, v78
	v_exp_f32_e32 v79, v79
	v_exp_f32_e32 v80, v80
	v_exp_f32_e32 v81, v81
	v_pk_add_f32 v[74:75], v[74:75], v[170:171] op_sel_hi:[1,0] neg_lo:[0,1] neg_hi:[0,1]
	v_pk_add_f32 v[96:97], v[82:83], 0 op_sel_hi:[1,0]
	v_pk_add_f32 v[76:77], v[76:77], v[170:171] op_sel_hi:[1,0] neg_lo:[0,1] neg_hi:[0,1]
	v_exp_f32_e32 v192, v74
	v_exp_f32_e32 v193, v75
	v_pk_add_f32 v[96:97], v[84:85], v[96:97]
	v_exp_f32_e32 v194, v76
	v_exp_f32_e32 v195, v77
	v_pk_add_f32 v[70:71], v[70:71], v[170:171] op_sel_hi:[1,0] neg_lo:[0,1] neg_hi:[0,1]
	v_pk_add_f32 v[74:75], v[78:79], v[96:97]
	v_pk_add_f32 v[72:73], v[72:73], v[170:171] op_sel_hi:[1,0] neg_lo:[0,1] neg_hi:[0,1]
	v_exp_f32_e32 v96, v70
	v_exp_f32_e32 v97, v71
	v_pk_add_f32 v[74:75], v[80:81], v[74:75]
	v_exp_f32_e32 v196, v72
	v_exp_f32_e32 v197, v73
	v_pk_add_f32 v[66:67], v[66:67], v[170:171] op_sel_hi:[1,0] neg_lo:[0,1] neg_hi:[0,1]
	v_pk_add_f32 v[74:75], v[192:193], v[74:75]
	v_pk_add_f32 v[68:69], v[68:69], v[170:171] op_sel_hi:[1,0] neg_lo:[0,1] neg_hi:[0,1]
	v_exp_f32_e32 v198, v66
	v_exp_f32_e32 v199, v67
	v_pk_add_f32 v[74:75], v[194:195], v[74:75]
	v_exp_f32_e32 v200, v68
	v_exp_f32_e32 v201, v69
	v_pk_add_f32 v[66:67], v[96:97], v[74:75]
	v_cvt_pk_bf16_f32 v68, v78, v79
	v_pk_add_f32 v[66:67], v[196:197], v[66:67]
	v_cvt_pk_bf16_f32 v69, v80, v81
	v_pk_add_f32 v[66:67], v[198:199], v[66:67]
	v_pk_add_f32 v[74:75], v[60:61], v[170:171] op_sel_hi:[1,0] neg_lo:[0,1] neg_hi:[0,1]
	v_pk_add_f32 v[202:203], v[200:201], v[66:67]
	v_cvt_pk_bf16_f32 v66, v82, v83
	v_cvt_pk_bf16_f32 v67, v84, v85
	v_pk_add_f32 v[76:77], v[62:63], v[170:171] op_sel_hi:[1,0] neg_lo:[0,1] neg_hi:[0,1]
	v_exp_f32_e32 v78, v74
	s_waitcnt lgkmcnt(14)
	v_mfma_f32_16x16x32_bf16 v[70:73], v[90:93], v[66:69], 0
	v_exp_f32_e32 v79, v75
	v_exp_f32_e32 v80, v76
	v_exp_f32_e32 v81, v77
	v_mfma_f32_16x16x32_bf16 v[60:63], v[86:89], v[66:69], 0
	v_add_f32_e64 v84, v56, -v170
	v_add_f32_e64 v85, v57, -v170
	v_pk_add_f32 v[86:87], v[58:59], v[170:171] op_sel_hi:[1,0] neg_lo:[0,1] neg_hi:[0,1]
	v_exp_f32_e32 v84, v84
	v_mfma_f32_16x16x32_bf16 v[74:77], v[100:103], v[66:69], 0
	v_exp_f32_e32 v85, v85
	v_exp_f32_e32 v86, v86
	v_exp_f32_e32 v87, v87
	v_mfma_f32_16x16x32_bf16 v[56:59], v[108:111], v[66:69], 0
	v_cvt_pk_bf16_f32 v66, v192, v193
	v_cvt_pk_bf16_f32 v67, v194, v195
	v_cvt_pk_bf16_f32 v68, v96, v97
	v_cvt_pk_bf16_f32 v69, v196, v197
	v_pk_add_f32 v[88:89], v[52:53], v[170:171] op_sel_hi:[1,0] neg_lo:[0,1] neg_hi:[0,1]
	v_pk_add_f32 v[82:83], v[78:79], v[202:203]
	v_mfma_f32_16x16x32_bf16 v[70:73], v[104:107], v[66:69], v[70:73]
	v_add_f32_e64 v90, v54, -v170
	v_add_f32_e64 v91, v55, -v170
	v_pk_add_f32 v[82:83], v[80:81], v[82:83]
	v_pk_add_f32 v[48:49], v[48:49], v[170:171] op_sel_hi:[1,0] neg_lo:[0,1] neg_hi:[0,1]
	v_mfma_f32_16x16x32_bf16 v[60:63], v[112:115], v[66:69], v[60:63]
	v_add_f32_e64 v82, v84, v82
	v_add_f32_e64 v83, v85, v83
	s_waitcnt lgkmcnt(1)
	v_mov_b32_e32 v100, v98
	v_pk_add_f32 v[82:83], v[86:87], v[82:83]
	v_mfma_f32_16x16x32_bf16 v[74:77], v[118:121], v[66:69], v[74:77]
	v_mov_b32_e32 v118, v116
	v_mov_b32_e32 v119, v117
	v_mov_b32_e32 v101, v99
	v_mfma_f32_16x16x32_bf16 v[52:55], v[126:129], v[66:69], v[56:59]
	s_waitcnt lgkmcnt(0)
	v_mov_b32_e32 v96, v94
	v_mov_b32_e32 v97, v95
	v_mov_b32_e32 v64, v65
	v_cvt_pk_bf16_f32 v58, v78, v79
	v_exp_f32_e32 v78, v88
	v_exp_f32_e32 v79, v89
	v_cvt_pk_bf16_f32 v56, v198, v199
	v_cvt_pk_bf16_f32 v57, v200, v201
	v_cvt_pk_bf16_f32 v59, v80, v81
	v_exp_f32_e32 v80, v90
	v_exp_f32_e32 v81, v91
	v_mfma_f32_16x16x32_bf16 v[66:69], v[122:125], v[56:59], v[70:73]
	v_add_f32_e64 v82, v78, v82
	v_add_f32_e64 v83, v79, v83
	s_cmp_eq_u32 s30, 1
	s_mov_b32 s23, 0xe800000
	v_mfma_f32_16x16x32_bf16 v[60:63], v[130:133], v[56:59], v[60:63]
	s_cselect_b32 s23, s23, 0x2e800000
	s_cmp_lg_u32 s30, 0
	s_cselect_b32 s23, s23, 0x12800000
	v_mfma_f32_16x16x32_bf16 v[70:73], v[138:141], v[56:59], v[74:77]
	s_add_u32 s36, s42, s23
	s_addc_u32 s37, s43, 0
	s_lshl_b32 s66, s22, 6
	v_pk_add_f32 v[74:75], v[50:51], v[170:171] op_sel_hi:[1,0] neg_lo:[0,1] neg_hi:[0,1]
	v_exp_f32_e32 v76, v48
	v_exp_f32_e32 v77, v49
	v_exp_f32_e32 v74, v74
	v_exp_f32_e32 v75, v75
	v_mfma_f32_16x16x32_bf16 v[48:51], v[146:149], v[56:59], v[52:55]
	s_nop 2
	v_cvt_pk_bf16_f32 v52, v84, v85
	v_cvt_pk_bf16_f32 v53, v86, v87
	v_cvt_pk_bf16_f32 v54, v78, v79
	v_cvt_pk_bf16_f32 v55, v80, v81
	v_pk_add_f32 v[78:79], v[80:81], v[82:83]
	s_nop 0
	v_mfma_f32_16x16x32_bf16 v[56:59], v[142:145], v[52:55], v[66:69]
	v_mfma_f32_16x16x32_bf16 v[66:69], v[152:155], v[52:55], v[60:63]
	v_mov_b32_e32 v152, v150
	v_mov_b32_e32 v153, v151
	s_nop 0
	v_pk_add_f32 v[60:61], v[76:77], v[78:79]
	v_mfma_f32_16x16x32_bf16 v[70:73], v[156:159], v[52:55], v[70:73]
	v_add_f32_e64 v60, v74, v60
	v_add_f32_e64 v61, v75, v61
	v_cvt_pk_bf16_f32 v62, v76, v77
	v_pk_add_f32 v[60:61], v[60:61], v[60:61] op_sel:[0,1] op_sel_hi:[1,0]
	v_mfma_f32_16x16x32_bf16 v[48:51], v[134:137], v[52:55], v[48:51]
	v_mov_b32_e32 v61, v60
	s_nop 1
	v_permlane16_swap_b32_e32 v60, v61
	v_cvt_pk_bf16_f32 v63, v74, v75
	v_add_f32_e32 v74, v60, v61
	s_nop 0
	v_mfma_f32_16x16x32_bf16 v[52:55], v[150:153], v[62:65], v[56:59]
	v_mfma_f32_16x16x32_bf16 v[56:59], v[116:119], v[62:65], v[66:69]
	v_mfma_f32_16x16x32_bf16 v[66:69], v[98:101], v[62:65], v[70:73]
	s_nop 2
	v_mov_b32_e32 v70, v74
	s_nop 1
	v_permlane32_swap_b32_e32 v74, v70
	v_mfma_f32_16x16x32_bf16 v[60:63], v[94:97], v[62:65], v[48:51]
	s_nop 2
	v_add_f32_e32 v48, v74, v70
	v_rcp_f32_e32 v49, v48
	s_nop 0
	v_mul_f32_e32 v49, 0x42800000, v49
	v_add3_u32 v206, s100, v177, v176
	s_waitcnt vmcnt(9)
	ds_write_b128 v206, v[16:19]
	v_mul_f32_e32 v50, v49, v52
	v_mul_f32_e32 v51, v49, v53
	v_med3_f32 v53, v50, s55, v228
	v_med3_f32 v51, v51, s55, v228
	v_mov_b32_e32 v50, v65
	v_cvt_pk_fp8_f32 v50, v53, v51
	s_waitcnt vmcnt(8)
	ds_write_b128 v206, v[20:23] offset:36864
	v_mul_f32_e32 v52, v49, v54
	v_mul_f32_e32 v51, v49, v55
	v_med3_f32 v52, v52, s55, v228
	v_med3_f32 v51, v51, s55, v228
	v_cvt_pk_fp8_f32 v50, v52, v51 op_sel:[0,0,1]
	v_add3_u32 v206, s100, v178, v176
	s_waitcnt vmcnt(7)
	ds_write_b128 v206, v[24:27]
	v_mul_f32_e32 v51, v49, v56
	v_mul_f32_e32 v52, v49, v57
	v_med3_f32 v54, v51, s55, v228
	v_med3_f32 v52, v52, s55, v228
	v_mov_b32_e32 v51, v65
	v_cvt_pk_fp8_f32 v51, v54, v52
	s_waitcnt vmcnt(6)
	ds_write_b128 v206, v[28:31] offset:36864
	v_mul_f32_e32 v53, v49, v58
	v_mul_f32_e32 v52, v49, v59
	v_med3_f32 v53, v53, s55, v228
	v_med3_f32 v52, v52, s55, v228
	v_cvt_pk_fp8_f32 v51, v53, v52 op_sel:[0,0,1]
	v_add3_u32 v206, s100, v179, v176
	s_waitcnt vmcnt(5)
	ds_write_b128 v206, v[32:35]
	v_mul_f32_e32 v52, v49, v66
	v_mul_f32_e32 v53, v49, v67
	v_med3_f32 v55, v52, s55, v228
	v_med3_f32 v53, v53, s55, v228
	v_mov_b32_e32 v52, v65
	v_cvt_pk_fp8_f32 v52, v55, v53
	s_waitcnt vmcnt(4)
	ds_write_b128 v206, v[36:39] offset:36864
	v_mul_f32_e32 v54, v49, v68
	v_mul_f32_e32 v53, v49, v69
	v_med3_f32 v54, v54, s55, v228
	v_med3_f32 v53, v53, s55, v228
	v_cvt_pk_fp8_f32 v52, v54, v53 op_sel:[0,0,1]
	v_add3_u32 v206, s100, v180, v176
	s_waitcnt vmcnt(3)
	ds_write_b128 v206, v[40:43]
	v_mul_f32_e32 v53, v49, v60
	v_mul_f32_e32 v54, v49, v61
	v_med3_f32 v56, v53, s55, v228
	v_med3_f32 v54, v54, s55, v228
	v_mov_b32_e32 v53, v65
	v_cvt_pk_fp8_f32 v53, v56, v54
	s_waitcnt vmcnt(2)
	ds_write_b128 v206, v[44:47] offset:36864
	v_mul_f32_e32 v55, v49, v62
	v_mul_f32_e32 v49, v49, v63
	v_med3_f32 v54, v55, s55, v228
	v_med3_f32 v49, v49, s55, v228
	v_cvt_pk_fp8_f32 v53, v54, v49 op_sel:[0,0,1]
	v_lshlrev_b64 v[54:55], 10, v[166:167]
	v_lshl_add_u64 v[54:55], s[36:37], 0, v[54:55]
	v_lshl_add_u64 v[54:55], v[54:55], 0, s[66:67]
	v_lshl_add_u64 v[54:55], v[54:55], 0, v[160:161]
	global_store_dwordx4 v[54:55], v[50:53], off sc1
	s_and_saveexec_b64 s[36:37], vcc
	s_cbranch_execz .LBB0_416
	v_log_f32_e32 v48, v48
	s_ashr_i32 s31, s30, 31
	s_lshl_b64 s[30:31], s[30:31], 22
	v_readlane_b32 s23, v254, 30
	s_add_u32 s30, s23, s30
	v_readlane_b32 s23, v254, 31
	v_add_f32_e32 v48, v170, v48
	s_addc_u32 s31, s23, s31
	v_mul_f32_e32 v50, 0x3f317218, v48
	v_lshlrev_b64 v[48:49], 6, v[166:167]
	v_lshl_add_u64 v[48:49], s[30:31], 0, v[48:49]
	s_mov_b32 s23, s67
	v_lshl_add_u64 v[48:49], s[22:23], 2, v[48:49]
	global_store_dword v[48:49], v50, off
.LBB0_416:
	s_or_b64 exec, exec, s[36:37]
	s_add_i32 s38, s38, 1
	s_and_b32 s22, s34, 15
	s_add_i32 s39, s39, 32
	s_cmpk_eq_i32 s38, 0x5f
	s_waitcnt lgkmcnt(0)
	s_barrier
	s_cbranch_scc1 .LBB0_418
	s_mov_b32 s30, s24
	v_mov_b64_e32 v[166:167], v[164:165]
	s_branch .LBB0_412
